# attention phases: one static s_setprio 1 for waves 4-7 (two waves per SIMD), reset at phase end
# speedup vs baseline: 1.0032x; 1.0020x over previous
; __device__ __forceinline__ void phase_pool(const Frame& F, bool dry) {
;     const bf16_t* UB = (const bf16_t*)(F.ws + AR_UB); bf16_t* PB = (bf16_t*)(F.ws + AR_PB);
;     const int gw = F.bid * NWAVES + F.wave, NGW = F.G * NWAVES, lane = F.lane;
;     for (int it = gw; it < 4 * (NTOK / 64); it += NGW) { const int g = it & 3, it4 = it >> 2; const int strip = 4 * it4 + (lane >> 4), ch = 16 * g + (lane & 15), t0 = strip * 16;
.LBB0_506:
	s_or_b64 exec, exec, s[0:1]
	s_xor_b64 s[0:1], s[34:35], -1
	v_writelane_b32 v255, s0, 24
	s_waitcnt lgkmcnt(0)
	s_barrier
	v_writelane_b32 v255, s1, 25
	v_readlane_b32 s0, v254, 17
	s_nop 1
	s_cmpk_le_i32 s0, 0xff00
	s_cbranch_scc0 .Lprio_a2
	s_setprio 1
.Lprio_a2:
	v_readlane_b32 s0, v253, 1
	v_readlane_b32 s1, v253, 2
	v_readlane_b32 s88, v253, 0
	v_writelane_b32 v255, s0, 26
	s_nop 1
	v_writelane_b32 v255, s1, 27
	s_mov_b32 s0, s93
	s_nop 0
	v_mbcnt_lo_u32_b32 v0, -1, s0
	v_readlane_b32 s0, v255, 20
	v_readlane_b32 s1, v255, 21
	s_mov_b32 s20, s0
	v_readlane_b32 s0, v254, 26
	v_readlane_b32 s1, v254, 27
	v_mbcnt_hi_u32_b32 v0, -1, v0
	v_add_u32_e32 v0, s94, v0
	v_cndmask_b32_e64 v1, 0, 1, s[0:1]
	v_cmp_ne_u32_e64 s[2:3], 1, v1
	s_andn2_b64 vcc, exec, s[0:1]
	v_and_b32_e32 v165, 63, v0
	v_writelane_b32 v255, s2, 28
	s_nop 1
	v_writelane_b32 v255, s3, 29
	s_cbranch_vccnz .LBB0_572
	v_lshlrev_b32_e32 v0, 3, v0
	v_and_b32_e32 v0, 0x78, v0
	v_readlane_b32 s0, v254, 35
	v_readlane_b32 s2, v254, 48
	s_nop 0
	v_or_b32_e32 v0, s0, v0
	v_readlane_b32 s0, v255, 26
	v_lshlrev_b32_e32 v112, 1, v0
	v_readlane_b32 s1, v255, 27
	s_nop 1
	v_lshl_add_u64 v[0:1], s[0:1], 0, v[112:113]
	s_mov_b64 s[0:1], 0xef00000
	v_lshl_add_u64 v[126:127], v[0:1], 0, s[0:1]
	s_mov_b64 s[0:1], 0x13f00000
	v_lshl_add_u64 v[128:129], v[0:1], 0, s[0:1]
	v_readlane_b32 s0, v255, 0
	s_mov_b32 s3, s0
	v_readlane_b32 s1, v255, 1
	s_branch .LBB0_510

; __device__ __forceinline__ int fresh_tid(int wave) { return wave * 64 + fresh_lane(); }
; __device__ __forceinline__ unsigned xb_ld(unsigned* p)              { return __hip_atomic_load(p, __ATOMIC_RELAXED, __HIP_MEMORY_SCOPE_AGENT); }
; __device__ __forceinline__ unsigned xb_add(unsigned* p, unsigned v) { return __hip_atomic_fetch_add(p, v, __ATOMIC_RELAXED, __HIP_MEMORY_SCOPE_AGENT); }
; __device__ __forceinline__ unsigned xb_xcc_id() { return (unsigned)__builtin_amdgcn_s_getreg((3 << 11) | 20) & 0xFu; }
; #define XB_SPIN(cond, bar) do { unsigned _sp = 0; while (cond) { __builtin_amdgcn_s_sleep(1); \
;     if ((++_sp & 255u) == 0u) { if (xb_ld(&(bar)[XB_TMO])) break; if (_sp > XB_SPIN_CAP) { atomicAdd(&(bar)[XB_TMO], 1u); break; } } } } while (0)
; __device__ __forceinline__ void xcd_barrier(const XcdBarrier& b) {
;     asm volatile("s_waitcnt vmcnt(0)" ::: "memory");
;     __syncthreads();
;     if (fresh_tid(b.wave) == 0) {
;         unsigned* bar = b.bar; asm volatile("" : "+s"(bar));
;         __builtin_amdgcn_s_waitcnt(0);
;         const unsigned bx = xb_xcc_id();
;         unsigned nloc = b.st[0], nx = b.st[1];
;         if (nloc == 0u) { xcd_barrier_complete(bar, bx, nloc, nx); b.st[0] = nloc; b.st[1] = nx; }
;         const unsigned old = xb_add(&bar[XB_XSUB(bx)], 1u);
;         const unsigned gen = old / nloc;
;         if (old + 1u == (gen + 1u) * nloc) {
;             __builtin_amdgcn_fence(__ATOMIC_RELEASE, "agent");
;             asm volatile("s_waitcnt vmcnt(0)" ::: "memory");
;             const unsigned og = xb_add(&bar[XB_TOP], 1u);
;             const unsigned tg = og / nx;
;             if (og + 1u == (tg + 1u) * nx) xb_add(&bar[XB_TOPGEN], 1u);
;             else XB_SPIN(xb_ld(&bar[XB_TOPGEN]) == tg, bar);
;             __builtin_amdgcn_fence(__ATOMIC_ACQUIRE, "agent");
;             xb_add(&bar[XB_XGEN(bx)], 1u);
.LBB0_903:
	s_setprio 0
	s_mov_b32 s0, s93
	s_waitcnt vmcnt(0) lgkmcnt(0)
	s_barrier
	s_waitcnt vmcnt(0)
	s_barrier
	s_nop 0
	v_mbcnt_lo_u32_b32 v0, -1, s0
	v_mbcnt_hi_u32_b32 v0, -1, v0
	v_readlane_b32 s0, v254, 17
	s_nop 1
	v_cmp_eq_u32_e32 vcc, s0, v0
	s_and_saveexec_b64 s[0:1], vcc
	s_cbranch_execz .LBB0_947
	s_bitcmp1_b32 s100, 0
	s_cbranch_scc0 .Lgb3_orig
	v_readlane_b32 s2, v253, 53
	v_readlane_b32 s3, v253, 54
	s_getreg_b32 s4, hwreg(HW_REG_XCC_ID, 0, 4)
	v_mov_b32_e32 v1, 1
	s_and_b32 s4, s4, 15
	s_lshl_b32 s4, s4, 8
	s_addk_i32 s4, 0x1400
	v_mov_b32_e32 v0, s4
	s_waitcnt vmcnt(0) lgkmcnt(0)
	global_atomic_add v2, v0, v1, s[2:3] sc0
	s_waitcnt vmcnt(0)
	v_readfirstlane_b32 s4, v2
	s_lshr_b32 s5, s4, 5
	s_and_b32 s4, s4, 31
	s_add_i32 s5, s5, 1
	s_lshl_b32 s5, s5, 3
	s_cmp_lg_u32 s4, 31
	s_cbranch_scc1 .Lgb3_poll
	buffer_wbl2 sc1
	s_waitcnt vmcnt(0)
	v_add_u32_e32 v0, 0x1000, v0
	global_atomic_add v0, v1, s[2:3]
	v_mov_b32_e32 v0, 0x3400
	global_atomic_add v2, v0, v1, s[2:3] sc0
	s_waitcnt vmcnt(0)
	v_readfirstlane_b32 s4, v2
	s_add_i32 s4, s4, 1
	s_cmp_lg_u32 s4, s5
	s_cbranch_scc1 .Lgb3_poll
	v_mov_b32_e32 v0, 0x3500
	global_atomic_add v0, v1, s[2:3]
	s_branch .Lgb3_done

; #define OPAQUE_WS() unsigned char* ws = P.ws; asm volatile("" : "+s"(ws)); F.ws = ws; F.tid = fresh_tid(F.wave); asm volatile("" : "+v"(F.tid)); F.lane = F.tid & 63; int c = F.bid; asm volatile("" : "+s"(c))
; #define REP_BEGIN(k) for (int rep_ = 0, nrep_ = ((k) >= PROBE_LO && (k) < PROBE_HI) ? PROBE_N : 0; rep_ <= nrep_; ++rep_) { const bool rerun = PROBE_AFTER ? (rep_ > 0) : (rep_ < nrep_), dry = rerun && PROBE_DRY_;
; __global__ void __launch_bounds__(NTHREADS, 2) mk_fwd(Params P) {
;     ...
;         if (PH_EN(5) && IN(pb + 5)) { REP_BEGIN(pb + 5) OPAQUE_WS(); int lq = l; asm volatile("" : "+s"(lq));
;     ...
;             att::XArgs A{(const bf16_t*)(ws + AR_QX), (const bf16_t*)(ws + WS_KXV) + (size_t)lq * B * MEM * 1024, (bf16_t*)(ws + AR_OX), P.in[20] + lq * XHD, dry};
;             for (int u = c, rnd = 0; u < B * XH * (S / 256); u += G, ++rnd) { int qt = u & 15, h = (u >> 4) & 3, b = u >> 6;
;                 if (G == 256) { const int idx = rnd * 32 + (c >> 3), bh = (c & 7) * 4 + (idx >> 4); qt = idx & 15; h = bh & 3; b = bh >> 2; }
;                 att::xattn_unit(A, b, h, qt, F.lds, F.wave); }
.LBB0_1221:
	s_or_b64 exec, exec, s[0:1]
	v_readlane_b32 s2, v253, 1
	v_readlane_b32 s3, v253, 2
	s_mov_b32 s0, s93
	s_waitcnt lgkmcnt(0)
	s_barrier
	v_readlane_b32 s18, v254, 17
	s_nop 1
	s_cmpk_le_i32 s18, 0xff00
	s_cbranch_scc0 .Lprio_x2
	s_setprio 1
.Lprio_x2:
	v_readlane_b32 s18, v253, 0
	v_mbcnt_lo_u32_b32 v0, -1, s0
	v_mbcnt_hi_u32_b32 v0, -1, v0
	v_add_u32_e32 v0, s94, v0
	v_readlane_b32 s4, v255, 20
	s_cmpk_gt_i32 s18, 0x1ff
	v_readlane_b32 s5, v255, 21
	s_cbranch_scc1 .LBB0_1237
	s_add_u32 s0, s2, 0x8f00000
	s_addc_u32 s1, s3, 0
	s_ashr_i32 s5, s4, 31
	s_lshl_b64 s[6:7], s[4:5], 22
	s_add_u32 s19, s2, s6
	s_addc_u32 s20, s3, s7
	s_add_u32 s21, s19, 0x700000
	s_addc_u32 s22, s20, 0
	s_add_u32 s23, s2, 0x8f00000
	s_addc_u32 s24, s3, 0
	s_lshl_b32 s2, s4, 7
	v_readlane_b32 s36, v253, 37
	s_ashr_i32 s3, s2, 31
	v_readlane_b32 s44, v253, 45
	v_readlane_b32 s45, v253, 46
	s_lshl_b64 s[2:3], s[2:3], 2
	v_readlane_b32 s46, v253, 47
	v_readlane_b32 s47, v253, 48
	s_mov_b64 s[8:9], s[44:45]
	s_add_u32 s2, s8, s2
	s_addc_u32 s3, s9, s3
	s_lshl_b32 s4, s18, 2
	s_ashr_i32 s25, s18, 3
	s_and_b32 s26, s4, 28
	s_add_u32 s6, s19, 0x740400
	s_addc_u32 s7, s20, 0
	s_mov_b32 s27, 0
	v_readlane_b32 s37, v253, 38
	v_readlane_b32 s38, v253, 39
	v_readlane_b32 s39, v253, 40
	v_readlane_b32 s40, v253, 41
	v_readlane_b32 s41, v253, 42
	v_readlane_b32 s42, v253, 43
	v_readlane_b32 s43, v253, 44
	v_readlane_b32 s48, v253, 49
	v_readlane_b32 s49, v253, 50
	v_readlane_b32 s50, v253, 51
	v_readlane_b32 s51, v253, 52
	s_mov_b64 s[10:11], s[46:47]
	s_branch .LBB0_1224

; __device__ __forceinline__ int fresh_tid(int wave) { return wave * 64 + fresh_lane(); }
; __device__ __forceinline__ unsigned xb_ld(unsigned* p)              { return __hip_atomic_load(p, __ATOMIC_RELAXED, __HIP_MEMORY_SCOPE_AGENT); }
; __device__ __forceinline__ unsigned xb_add(unsigned* p, unsigned v) { return __hip_atomic_fetch_add(p, v, __ATOMIC_RELAXED, __HIP_MEMORY_SCOPE_AGENT); }
; __device__ __forceinline__ unsigned xb_xcc_id() { return (unsigned)__builtin_amdgcn_s_getreg((3 << 11) | 20) & 0xFu; }
; #define XB_SPIN(cond, bar) do { unsigned _sp = 0; while (cond) { __builtin_amdgcn_s_sleep(1); \
;     if ((++_sp & 255u) == 0u) { if (xb_ld(&(bar)[XB_TMO])) break; if (_sp > XB_SPIN_CAP) { atomicAdd(&(bar)[XB_TMO], 1u); break; } } } } while (0)
; __device__ __forceinline__ void xcd_barrier(const XcdBarrier& b) {
;     asm volatile("s_waitcnt vmcnt(0)" ::: "memory");
;     __syncthreads();
;     if (fresh_tid(b.wave) == 0) {
;         unsigned* bar = b.bar; asm volatile("" : "+s"(bar));
;         __builtin_amdgcn_s_waitcnt(0);
;         const unsigned bx = xb_xcc_id();
;         unsigned nloc = b.st[0], nx = b.st[1];
;         if (nloc == 0u) { xcd_barrier_complete(bar, bx, nloc, nx); b.st[0] = nloc; b.st[1] = nx; }
;         const unsigned old = xb_add(&bar[XB_XSUB(bx)], 1u);
;         const unsigned gen = old / nloc;
;         if (old + 1u == (gen + 1u) * nloc) {
;             __builtin_amdgcn_fence(__ATOMIC_RELEASE, "agent");
;             asm volatile("s_waitcnt vmcnt(0)" ::: "memory");
;             const unsigned og = xb_add(&bar[XB_TOP], 1u);
;             const unsigned tg = og / nx;
;             if (og + 1u == (tg + 1u) * nx) xb_add(&bar[XB_TOPGEN], 1u);
;             else XB_SPIN(xb_ld(&bar[XB_TOPGEN]) == tg, bar);
;             __builtin_amdgcn_fence(__ATOMIC_ACQUIRE, "agent");
;             xb_add(&bar[XB_XGEN(bx)], 1u);
.LBB0_1237:
	s_setprio 0
	s_mov_b32 s0, s93
	s_waitcnt lgkmcnt(0)
	s_barrier
	s_waitcnt vmcnt(0)
	s_barrier
	s_nop 0
	v_mbcnt_lo_u32_b32 v0, -1, s0
	v_mbcnt_hi_u32_b32 v0, -1, v0
	v_readlane_b32 s0, v254, 17
	s_nop 1
	v_cmp_eq_u32_e32 vcc, s0, v0
	s_and_saveexec_b64 s[0:1], vcc
	s_cbranch_execz .LBB0_1281
	s_bitcmp1_b32 s100, 0
	s_cbranch_scc0 .Llb_x2_glob
	v_readlane_b32 s2, v253, 53
	v_readlane_b32 s3, v253, 54
	v_readlane_b32 s4, v253, 0
	v_mov_b32_e32 v1, 1
	s_and_b32 s4, s4, 7
	s_lshl_b32 s4, s4, 8
	s_addk_i32 s4, 0x480
	v_mov_b32_e32 v0, s4
	s_waitcnt vmcnt(0) lgkmcnt(0)
	global_atomic_add v0, v1, s[2:3]
	s_add_i32 s101, s101, 32
	s_mov_b32 s5, 0
	v_mov_b32_e32 v2, s101
